# baseline (speedup 1.0000x reference)
amdhsa.kernels:
  - .agpr_count:     0
    .args:
      - .actual_access:  read_only
        .address_space:  global
        .offset:         0
        .size:           8
        .value_kind:     global_buffer
      - .actual_access:  read_only
        .address_space:  global
        .offset:         8
        .size:           8
        .value_kind:     global_buffer
      - .actual_access:  read_only
        .address_space:  global
        .offset:         16
        .size:           8
        .value_kind:     global_buffer
      - .actual_access:  write_only
        .address_space:  global
        .offset:         24
        .size:           8
        .value_kind:     global_buffer
      - .actual_access:  write_only
        .address_space:  global
        .offset:         32
        .size:           8
        .value_kind:     global_buffer
    .group_segment_fixed_size: 0
    .kernarg_segment_align: 8
    .kernarg_segment_size: 40
    .language:       OpenCL C
    .language_version:
      - 2
      - 0
    .max_flat_workgroup_size: 256
    .name:           _Z12wprep_kernelPKfS0_S0_PDF16_Pj
    .private_segment_fixed_size: 0
    .sgpr_count:     18
    .sgpr_spill_count: 0
    .symbol:         _Z12wprep_kernelPKfS0_S0_PDF16_Pj.kd
    .uniform_work_group_size: 1
    .uses_dynamic_stack: false
    .vgpr_count:     12
    .vgpr_spill_count: 0
    .wavefront_size: 64
  - .agpr_count:     0
    .args:
      - .actual_access:  read_only
        .address_space:  global
        .offset:         0
        .size:           8
        .value_kind:     global_buffer
      - .actual_access:  read_only
        .address_space:  global
        .offset:         8
        .size:           8
        .value_kind:     global_buffer
      - .actual_access:  read_only
        .address_space:  global
        .offset:         16
        .size:           8
        .value_kind:     global_buffer
      - .actual_access:  read_only
        .address_space:  global
        .offset:         24
        .size:           8
        .value_kind:     global_buffer
      - .actual_access:  read_only
        .address_space:  global
        .offset:         32
        .size:           8
        .value_kind:     global_buffer
      - .actual_access:  read_only
        .address_space:  global
        .offset:         40
        .size:           8
        .value_kind:     global_buffer
      - .actual_access:  read_only
        .address_space:  global
        .offset:         48
        .size:           8
        .value_kind:     global_buffer
      - .actual_access:  write_only
        .address_space:  global
        .offset:         56
        .size:           8
        .value_kind:     global_buffer
      - .actual_access:  write_only
        .address_space:  global
        .offset:         64
        .size:           8
        .value_kind:     global_buffer
      - .actual_access:  write_only
        .address_space:  global
        .offset:         72
        .size:           8
        .value_kind:     global_buffer
      - .address_space:  global
        .offset:         80
        .size:           8
        .value_kind:     global_buffer
    .group_segment_fixed_size: 0
    .kernarg_segment_align: 8
    .kernarg_segment_size: 88
    .language:       OpenCL C
    .language_version:
      - 2
      - 0
    .max_flat_workgroup_size: 512
    .name:           _Z11proj_kernelPKfS0_S0_PKDF16_S0_S0_S0_PDF16_S3_S3_Pj
    .private_segment_fixed_size: 0
    .sgpr_count:     51
    .sgpr_spill_count: 0
    .symbol:         _Z11proj_kernelPKfS0_S0_PKDF16_S0_S0_S0_PDF16_S3_S3_Pj.kd
    .uniform_work_group_size: 1
    .uses_dynamic_stack: false
    .vgpr_count:     248
    .vgpr_spill_count: 0
    .wavefront_size: 64
  - .agpr_count:     0
    .args:
      - .actual_access:  read_only
        .address_space:  global
        .offset:         0
        .size:           8
        .value_kind:     global_buffer
      - .address_space:  global
        .offset:         8
        .size:           8
        .value_kind:     global_buffer
      - .address_space:  global
        .offset:         16
        .size:           8
        .value_kind:     global_buffer
      - .actual_access:  read_only
        .address_space:  global
        .offset:         24
        .size:           8
        .value_kind:     global_buffer
      - .actual_access:  write_only
        .address_space:  global
        .offset:         32
        .size:           8
        .value_kind:     global_buffer
    .group_segment_fixed_size: 0
    .kernarg_segment_align: 8
    .kernarg_segment_size: 40
    .language:       OpenCL C
    .language_version:
      - 2
      - 0
    .max_flat_workgroup_size: 512
    .name:           _Z11attn_kernelPKDF16_S0_S0_PKjPf
    .private_segment_fixed_size: 0
    .sgpr_count:     50
    .sgpr_spill_count: 0
    .symbol:         _Z11attn_kernelPKDF16_S0_S0_PKjPf.kd
    .uniform_work_group_size: 1
    .uses_dynamic_stack: false
    .vgpr_count:     192
    .vgpr_spill_count: 0
    .wavefront_size: 64
